# attention unit end: store drain (vmcnt 0) before the unit-end barrier removed; the next unit's first wait or the seam drains the O stores
# baseline (speedup 1.0000x reference)
.LBB0_1569:
	s_or_b64 exec, exec, s[2:3]
	s_waitcnt lgkmcnt(0)
	v_add_u32_e32 v2, v2, v153
	ds_read_b128 v[36:39], v2
	ds_read_b128 v[40:43], v2 offset:32
	v_ashrrev_i32_e32 v44, 6, v150
	v_readlane_b32 s2, v255, 11
	v_lshlrev_b32_e32 v54, 9, v151
	s_waitcnt lgkmcnt(1)
	v_rcp_f32_e32 v45, v36
	v_rcp_f32_e32 v46, v37
	v_rcp_f32_e32 v47, v38
	v_rcp_f32_e32 v48, v39
	ds_read_b128 v[36:39], v2 offset:64
	s_waitcnt lgkmcnt(1)
	v_rcp_f32_e32 v49, v40
	v_rcp_f32_e32 v50, v41
	v_rcp_f32_e32 v51, v42
	v_rcp_f32_e32 v52, v43
	ds_read_b128 v[40:43], v2 offset:96
	s_waitcnt lgkmcnt(1)
	v_rcp_f32_e32 v2, v36
	v_lshlrev_b32_e32 v36, 5, v44
	v_lshl_add_u32 v44, v44, 12, s2
	v_lshlrev_b32_e32 v55, 1, v137
	v_mul_f32_e32 v4, v4, v45
	v_add3_u32 v54, v44, v54, v55
	v_cvt_pk_bf16_f32 v4, v4, v3
	ds_write_b16 v54, v4
	v_mul_f32_e32 v4, v20, v45
	v_cvt_pk_bf16_f32 v4, v4, v3
	ds_write_b16 v54, v4 offset:64
	v_mul_f32_e32 v4, v5, v46
	v_cvt_pk_bf16_f32 v4, v4, v3
	ds_write_b16 v54, v4 offset:128
	v_mul_f32_e32 v4, v21, v46
	v_cvt_pk_bf16_f32 v4, v4, v3
	ds_write_b16 v54, v4 offset:192
	v_mul_f32_e32 v4, v6, v47
	v_cvt_pk_bf16_f32 v4, v4, v3
	ds_write_b16 v54, v4 offset:256
	v_mul_f32_e32 v4, v22, v47
	v_cvt_pk_bf16_f32 v4, v4, v3
	ds_write_b16 v54, v4 offset:320
	v_mul_f32_e32 v4, v7, v48
	v_cvt_pk_bf16_f32 v4, v4, v3
	ds_write_b16 v54, v4 offset:384
	v_mul_f32_e32 v4, v23, v48
	v_cvt_pk_bf16_f32 v4, v4, v3
	ds_write_b16 v54, v4 offset:448
	v_mul_f32_e32 v4, v8, v49
	v_cvt_pk_bf16_f32 v4, v4, v3
	ds_write_b16 v54, v4 offset:1024
	v_mul_f32_e32 v4, v24, v49
	v_cvt_pk_bf16_f32 v4, v4, v3
	ds_write_b16 v54, v4 offset:1088
	v_mul_f32_e32 v4, v9, v50
	v_cvt_pk_bf16_f32 v4, v4, v3
	ds_write_b16 v54, v4 offset:1152
	v_mul_f32_e32 v4, v25, v50
	v_cvt_pk_bf16_f32 v4, v4, v3
	ds_write_b16 v54, v4 offset:1216
	v_mul_f32_e32 v4, v10, v51
	v_cvt_pk_bf16_f32 v4, v4, v3
	ds_write_b16 v54, v4 offset:1280
	v_mul_f32_e32 v4, v26, v51
	v_cvt_pk_bf16_f32 v4, v4, v3
	ds_write_b16 v54, v4 offset:1344
	v_mul_f32_e32 v4, v11, v52
	v_cvt_pk_bf16_f32 v4, v4, v3
	v_rcp_f32_e32 v53, v37
	ds_write_b16 v54, v4 offset:1408
	v_mul_f32_e32 v4, v27, v52
	v_cvt_pk_bf16_f32 v4, v4, v3
	ds_write_b16 v54, v4 offset:1472
	v_mul_f32_e32 v4, v12, v2
	v_mul_f32_e32 v2, v28, v2
	v_cvt_pk_bf16_f32 v4, v4, v3
	ds_write_b16 v54, v4 offset:2048
	v_cvt_pk_bf16_f32 v2, v2, v3
	v_rcp_f32_e32 v38, v38
	ds_write_b16 v54, v2 offset:2112
	v_mul_f32_e32 v2, v13, v53
	v_cvt_pk_bf16_f32 v2, v2, v3
	ds_write_b16 v54, v2 offset:2176
	v_mul_f32_e32 v2, v29, v53
	v_cvt_pk_bf16_f32 v2, v2, v3
	v_rcp_f32_e32 v39, v39
	ds_write_b16 v54, v2 offset:2240
	v_mul_f32_e32 v2, v14, v38
	v_cvt_pk_bf16_f32 v2, v2, v3
	ds_write_b16 v54, v2 offset:2304
	v_mul_f32_e32 v2, v30, v38
	v_cvt_pk_bf16_f32 v2, v2, v3
	s_waitcnt lgkmcnt(14)
	v_rcp_f32_e32 v40, v40
	ds_write_b16 v54, v2 offset:2368
	v_mul_f32_e32 v2, v15, v39
	v_cvt_pk_bf16_f32 v2, v2, v3
	ds_write_b16 v54, v2 offset:2432
	v_mul_f32_e32 v2, v31, v39
	v_cvt_pk_bf16_f32 v2, v2, v3
	v_rcp_f32_e32 v41, v41
	ds_write_b16 v54, v2 offset:2496
	v_mul_f32_e32 v2, v16, v40
	v_cvt_pk_bf16_f32 v2, v2, v3
	ds_write_b16 v54, v2 offset:3072
	v_mul_f32_e32 v2, v32, v40
	v_cvt_pk_bf16_f32 v2, v2, v3
	v_rcp_f32_e32 v42, v42
	ds_write_b16 v54, v2 offset:3136
	v_mul_f32_e32 v2, v17, v41
	v_cvt_pk_bf16_f32 v2, v2, v3
	ds_write_b16 v54, v2 offset:3200
	v_mul_f32_e32 v2, v33, v41
	v_cvt_pk_bf16_f32 v2, v2, v3
	v_rcp_f32_e32 v43, v43
	ds_write_b16 v54, v2 offset:3264
	v_mul_f32_e32 v2, v18, v42
	v_cvt_pk_bf16_f32 v2, v2, v3
	ds_write_b16 v54, v2 offset:3328
	v_mul_f32_e32 v2, v34, v42
	v_cvt_pk_bf16_f32 v2, v2, v3
	v_ashrrev_i32_e32 v37, 31, v36
	ds_write_b16 v54, v2 offset:3392
	v_mul_f32_e32 v2, v19, v43
	v_lshl_add_u64 v[36:37], s[16:17], 0, v[36:37]
	v_cvt_pk_bf16_f32 v2, v2, v3
	v_lshlrev_b64 v[36:37], 10, v[36:37]
	ds_write_b16 v54, v2 offset:3456
	v_mul_f32_e32 v2, v35, v43
	v_cvt_pk_bf16_f32 v2, v2, v3
	ds_write_b16 v54, v2 offset:3520
	v_lshl_add_u64 v[4:5], s[12:13], 0, v[36:37]
	s_lshl_b32 s34, s51, 1
	v_lshrrev_b32_e32 v16, 3, v152
	v_add_u32_e32 v17, v44, v136
	v_lshl_add_u64 v[4:5], v[4:5], 0, s[34:35]
	s_waitcnt lgkmcnt(0)
	v_mov_b32_e32 v137, v3
	v_lshl_add_u32 v2, v16, 7, v17
	v_or_b32_e32 v18, 8, v16
	v_lshl_add_u64 v[12:13], v[4:5], 0, v[136:137]
	ds_read_b128 v[4:7], v2
	v_lshl_add_u32 v8, v18, 7, v17
	ds_read_b128 v[8:11], v8
	v_lshlrev_b32_e32 v2, 10, v16
	v_lshl_add_u64 v[14:15], v[12:13], 0, v[2:3]
	v_lshlrev_b32_e32 v2, 10, v18
	s_waitcnt lgkmcnt(1)
	global_store_dwordx4 v[14:15], v[4:7], off
	s_nop 1
	v_lshl_add_u64 v[4:5], v[12:13], 0, v[2:3]
	v_or_b32_e32 v2, 16, v16
	s_waitcnt lgkmcnt(0)
	global_store_dwordx4 v[4:5], v[8:11], off
	v_lshl_add_u32 v4, v2, 7, v17
	v_or_b32_e32 v16, 24, v16
	ds_read_b128 v[4:7], v4
	v_lshl_add_u32 v8, v16, 7, v17
	ds_read_b128 v[8:11], v8
	v_lshlrev_b32_e32 v2, 10, v2
	v_lshl_add_u64 v[14:15], v[12:13], 0, v[2:3]
	v_lshlrev_b32_e32 v2, 10, v16
	s_waitcnt lgkmcnt(1)
	global_store_dwordx4 v[14:15], v[4:7], off
	s_nop 1
	v_lshl_add_u64 v[4:5], v[12:13], 0, v[2:3]
	s_waitcnt lgkmcnt(0)
	global_store_dwordx4 v[4:5], v[8:11], off
	s_waitcnt lgkmcnt(0)
	s_barrier

.LBB0_1611:
	v_cndmask_b32_e64 v70, v70, v108, s[2:3]
	v_sub_f32_e32 v52, v52, v70
	v_sub_f32_e32 v53, v53, v70
	v_exp_f32_e32 v52, v52
	v_sub_f32_e32 v54, v54, v70
	v_exp_f32_e32 v53, v53
	v_sub_f32_e32 v55, v55, v70
	v_exp_f32_e32 v54, v54
	v_sub_f32_e32 v56, v56, v70
	v_sub_f32_e32 v36, v36, v70
	v_exp_f32_e32 v55, v55
	v_sub_f32_e32 v57, v57, v70
	v_sub_f32_e32 v58, v58, v70
	v_sub_f32_e32 v59, v59, v70
	v_sub_f32_e32 v60, v60, v70
	v_sub_f32_e32 v61, v61, v70
	v_sub_f32_e32 v62, v62, v70
	v_sub_f32_e32 v63, v63, v70
	v_sub_f32_e32 v64, v64, v70
	v_sub_f32_e32 v65, v65, v70
	v_sub_f32_e32 v66, v66, v70
	v_sub_f32_e32 v67, v67, v70
	v_sub_f32_e32 v37, v37, v70
	v_sub_f32_e32 v38, v38, v70
	v_sub_f32_e32 v39, v39, v70
	v_sub_f32_e32 v40, v40, v70
	v_sub_f32_e32 v41, v41, v70
	v_sub_f32_e32 v42, v42, v70
	v_sub_f32_e32 v43, v43, v70
	v_sub_f32_e32 v44, v44, v70
	v_sub_f32_e32 v45, v45, v70
	v_sub_f32_e32 v46, v46, v70
	v_sub_f32_e32 v47, v47, v70
	v_sub_f32_e32 v48, v48, v70
	v_sub_f32_e32 v49, v49, v70
	v_sub_f32_e32 v50, v50, v70
	v_sub_f32_e32 v51, v51, v70
	v_exp_f32_e32 v56, v56
	v_exp_f32_e32 v70, v36
	v_add_f32_e32 v36, 0, v52
	v_exp_f32_e32 v57, v57
	v_add_f32_e32 v36, v53, v36
	v_exp_f32_e32 v58, v58
	v_add_f32_e32 v36, v54, v36
	v_exp_f32_e32 v59, v59
	v_add_f32_e32 v36, v55, v36
	v_exp_f32_e32 v60, v60
	v_add_f32_e32 v36, v56, v36
	v_exp_f32_e32 v61, v61
	v_add_f32_e32 v36, v57, v36
	v_exp_f32_e32 v62, v62
	v_add_f32_e32 v36, v58, v36
	v_exp_f32_e32 v63, v63
	v_add_f32_e32 v36, v59, v36
	v_exp_f32_e32 v64, v64
	v_add_f32_e32 v36, v60, v36
	v_exp_f32_e32 v65, v65
	v_add_f32_e32 v36, v61, v36
	v_exp_f32_e32 v66, v66
	v_add_f32_e32 v36, v62, v36
	v_exp_f32_e32 v67, v67
	v_add_f32_e32 v36, v63, v36
	v_add_f32_e32 v36, v64, v36
	v_exp_f32_e32 v71, v37
	v_add_f32_e32 v36, v65, v36
	v_exp_f32_e32 v72, v38
	v_add_f32_e32 v36, v66, v36
	v_exp_f32_e32 v73, v39
	v_add_f32_e32 v36, v67, v36
	v_exp_f32_e32 v74, v40
	v_add_f32_e32 v36, v70, v36
	v_exp_f32_e32 v75, v41
	v_add_f32_e32 v36, v71, v36
	v_exp_f32_e32 v76, v42
	v_add_f32_e32 v36, v72, v36
	v_exp_f32_e32 v77, v43
	v_add_f32_e32 v36, v73, v36
	v_exp_f32_e32 v78, v44
	v_add_f32_e32 v36, v74, v36
	v_exp_f32_e32 v79, v45
	v_add_f32_e32 v36, v75, v36
	v_exp_f32_e32 v82, v46
	v_add_f32_e32 v36, v76, v36
	v_exp_f32_e32 v83, v47
	v_add_f32_e32 v36, v77, v36
	v_exp_f32_e32 v108, v48
	v_add_f32_e32 v36, v78, v36
	v_exp_f32_e32 v110, v49
	v_add_f32_e32 v36, v79, v36
	v_exp_f32_e32 v111, v50
	v_add_f32_e32 v36, v82, v36
	v_exp_f32_e32 v112, v51
	v_add_f32_e32 v36, v83, v36
	v_add_f32_e32 v36, v108, v36
	v_add_f32_e32 v36, v110, v36
	v_add_f32_e32 v36, v111, v36
	v_add_f32_e32 v36, v112, v36
	v_mov_b32_e32 v37, v36
	s_nop 1
	v_permlane32_swap_b32_e32 v36, v37
	v_cvt_pk_bf16_f32 v38, v52, v53
	v_cvt_pk_bf16_f32 v39, v54, v55
	v_cvt_pk_bf16_f32 v40, v56, v57
	v_cvt_pk_bf16_f32 v41, v58, v59
	v_cvt_pk_bf16_f32 v42, v60, v61
	v_cvt_pk_bf16_f32 v43, v62, v63
	v_cvt_pk_bf16_f32 v44, v64, v65
	v_cvt_pk_bf16_f32 v45, v66, v67
	v_cvt_pk_bf16_f32 v46, v70, v71
	v_cvt_pk_bf16_f32 v47, v72, v73
	v_cvt_pk_bf16_f32 v48, v74, v75
	v_cvt_pk_bf16_f32 v49, v76, v77
	v_cvt_pk_bf16_f32 v50, v78, v79
	v_cvt_pk_bf16_f32 v51, v82, v83
	v_cvt_pk_bf16_f32 v52, v108, v110
	v_cvt_pk_bf16_f32 v53, v111, v112
	s_nop 0
	v_permlane32_swap_b32_e32 v38, v40
	v_permlane32_swap_b32_e32 v39, v41
	v_permlane32_swap_b32_e32 v42, v44
	v_permlane32_swap_b32_e32 v43, v45
	v_permlane32_swap_b32_e32 v46, v48
	v_permlane32_swap_b32_e32 v47, v49
	v_permlane32_swap_b32_e32 v50, v52
	v_permlane32_swap_b32_e32 v51, v53
	ds_read_b64_tr_b16 v[54:55], v140 offset:0
	ds_read_b64_tr_b16 v[56:57], v140 offset:0x400
	ds_read_b64_tr_b16 v[58:59], v140 offset:0x800
	ds_read_b64_tr_b16 v[60:61], v140 offset:0xc00
	ds_read_b64_tr_b16 v[62:63], v140 offset:0x1000
	ds_read_b64_tr_b16 v[64:65], v140 offset:0x1400
	ds_read_b64_tr_b16 v[70:71], v140 offset:0x1800
	ds_read_b64_tr_b16 v[72:73], v140 offset:0x1c00
	s_waitcnt lgkmcnt(0)
	s_nop 0
	v_mfma_f32_32x32x16_bf16 v[4:19], v[38:41], v[54:57], v[4:19]
	ds_read_b64_tr_b16 v[54:55], v140 offset:0x200
	ds_read_b64_tr_b16 v[56:57], v140 offset:0x600
	v_mfma_f32_32x32x16_bf16 v[4:19], v[42:45], v[58:61], v[4:19]
	ds_read_b64_tr_b16 v[58:59], v140 offset:0xa00
	ds_read_b64_tr_b16 v[60:61], v140 offset:0xe00
	v_mfma_f32_32x32x16_bf16 v[4:19], v[46:49], v[62:65], v[4:19]
	ds_read_b64_tr_b16 v[62:63], v140 offset:0x1200
	ds_read_b64_tr_b16 v[64:65], v140 offset:0x1600
	v_mfma_f32_32x32x16_bf16 v[4:19], v[50:53], v[70:73], v[4:19]
	ds_read_b64_tr_b16 v[70:71], v140 offset:0x1a00
	ds_read_b64_tr_b16 v[72:73], v140 offset:0x1e00
	s_waitcnt lgkmcnt(0)
	v_mfma_f32_32x32x16_bf16 v[20:35], v[38:41], v[54:57], v[20:35]
	v_mfma_f32_32x32x16_bf16 v[20:35], v[42:45], v[58:61], v[20:35]
	v_mfma_f32_32x32x16_bf16 v[20:35], v[46:49], v[62:65], v[20:35]
	v_mfma_f32_32x32x16_bf16 v[20:35], v[50:53], v[70:73], v[20:35]
	s_and_saveexec_b64 s[2:3], s[38:39]
	v_add_f32_e32 v2, v2, v68
	v_fmac_f32_e32 v2, v142, v178
	v_add_f32_e32 v36, v36, v37
	v_fmac_f32_e32 v36, v2, v69
	ds_write_b32 v141, v36
	s_or_b64 exec, exec, s[2:3]
	s_waitcnt lgkmcnt(0)
	v_add_u32_e32 v2, v139, v137
	ds_read_b128 v[36:39], v2
	ds_read_b128 v[40:43], v2 offset:32
	v_ashrrev_i32_e32 v44, 6, v109
	v_readlane_b32 s2, v255, 11
	v_lshlrev_b32_e32 v54, 9, v136
	s_waitcnt lgkmcnt(1)
	v_rcp_f32_e32 v45, v36
	v_rcp_f32_e32 v46, v37
	v_rcp_f32_e32 v47, v38
	v_rcp_f32_e32 v48, v39
	ds_read_b128 v[36:39], v2 offset:64
	s_waitcnt lgkmcnt(1)
	v_rcp_f32_e32 v49, v40
	v_rcp_f32_e32 v50, v41
	v_rcp_f32_e32 v51, v42
	v_rcp_f32_e32 v52, v43
	ds_read_b128 v[40:43], v2 offset:96
	s_waitcnt lgkmcnt(1)
	v_rcp_f32_e32 v2, v36
	v_lshlrev_b32_e32 v36, 5, v44
	v_lshl_add_u32 v44, v44, 12, s2
	v_lshlrev_b32_e32 v55, 1, v81
	v_mul_f32_e32 v4, v4, v45
	v_add3_u32 v54, v44, v54, v55
	v_cvt_pk_bf16_f32 v4, v4, v3
	ds_write_b16 v54, v4
	v_mul_f32_e32 v4, v20, v45
	v_cvt_pk_bf16_f32 v4, v4, v3
	ds_write_b16 v54, v4 offset:64
	v_mul_f32_e32 v4, v5, v46
	v_cvt_pk_bf16_f32 v4, v4, v3
	ds_write_b16 v54, v4 offset:128
	v_mul_f32_e32 v4, v21, v46
	v_cvt_pk_bf16_f32 v4, v4, v3
	ds_write_b16 v54, v4 offset:192
	v_mul_f32_e32 v4, v6, v47
	v_cvt_pk_bf16_f32 v4, v4, v3
	ds_write_b16 v54, v4 offset:256
	v_mul_f32_e32 v4, v22, v47
	v_cvt_pk_bf16_f32 v4, v4, v3
	ds_write_b16 v54, v4 offset:320
	v_mul_f32_e32 v4, v7, v48
	v_cvt_pk_bf16_f32 v4, v4, v3
	ds_write_b16 v54, v4 offset:384
	v_mul_f32_e32 v4, v23, v48
	v_cvt_pk_bf16_f32 v4, v4, v3
	ds_write_b16 v54, v4 offset:448
	v_mul_f32_e32 v4, v8, v49
	v_cvt_pk_bf16_f32 v4, v4, v3
	ds_write_b16 v54, v4 offset:1024
	v_mul_f32_e32 v4, v24, v49
	v_cvt_pk_bf16_f32 v4, v4, v3
	ds_write_b16 v54, v4 offset:1088
	v_mul_f32_e32 v4, v9, v50
	v_cvt_pk_bf16_f32 v4, v4, v3
	ds_write_b16 v54, v4 offset:1152
	v_mul_f32_e32 v4, v25, v50
	v_cvt_pk_bf16_f32 v4, v4, v3
	ds_write_b16 v54, v4 offset:1216
	v_mul_f32_e32 v4, v10, v51
	v_cvt_pk_bf16_f32 v4, v4, v3
	ds_write_b16 v54, v4 offset:1280
	v_mul_f32_e32 v4, v26, v51
	v_cvt_pk_bf16_f32 v4, v4, v3
	ds_write_b16 v54, v4 offset:1344
	v_mul_f32_e32 v4, v11, v52
	v_cvt_pk_bf16_f32 v4, v4, v3
	v_rcp_f32_e32 v53, v37
	ds_write_b16 v54, v4 offset:1408
	v_mul_f32_e32 v4, v27, v52
	v_cvt_pk_bf16_f32 v4, v4, v3
	ds_write_b16 v54, v4 offset:1472
	v_mul_f32_e32 v4, v12, v2
	v_mul_f32_e32 v2, v28, v2
	v_cvt_pk_bf16_f32 v4, v4, v3
	ds_write_b16 v54, v4 offset:2048
	v_cvt_pk_bf16_f32 v2, v2, v3
	v_rcp_f32_e32 v38, v38
	ds_write_b16 v54, v2 offset:2112
	v_mul_f32_e32 v2, v13, v53
	v_cvt_pk_bf16_f32 v2, v2, v3
	ds_write_b16 v54, v2 offset:2176
	v_mul_f32_e32 v2, v29, v53
	v_cvt_pk_bf16_f32 v2, v2, v3
	v_rcp_f32_e32 v39, v39
	ds_write_b16 v54, v2 offset:2240
	v_mul_f32_e32 v2, v14, v38
	v_cvt_pk_bf16_f32 v2, v2, v3
	ds_write_b16 v54, v2 offset:2304
	v_mul_f32_e32 v2, v30, v38
	v_cvt_pk_bf16_f32 v2, v2, v3
	s_waitcnt lgkmcnt(14)
	v_rcp_f32_e32 v40, v40
	ds_write_b16 v54, v2 offset:2368
	v_mul_f32_e32 v2, v15, v39
	v_cvt_pk_bf16_f32 v2, v2, v3
	ds_write_b16 v54, v2 offset:2432
	v_mul_f32_e32 v2, v31, v39
	v_cvt_pk_bf16_f32 v2, v2, v3
	v_rcp_f32_e32 v41, v41
	ds_write_b16 v54, v2 offset:2496
	v_mul_f32_e32 v2, v16, v40
	v_cvt_pk_bf16_f32 v2, v2, v3
	ds_write_b16 v54, v2 offset:3072
	v_mul_f32_e32 v2, v32, v40
	v_cvt_pk_bf16_f32 v2, v2, v3
	v_rcp_f32_e32 v42, v42
	ds_write_b16 v54, v2 offset:3136
	v_mul_f32_e32 v2, v17, v41
	v_cvt_pk_bf16_f32 v2, v2, v3
	ds_write_b16 v54, v2 offset:3200
	v_mul_f32_e32 v2, v33, v41
	v_cvt_pk_bf16_f32 v2, v2, v3
	v_rcp_f32_e32 v43, v43
	ds_write_b16 v54, v2 offset:3264
	v_mul_f32_e32 v2, v18, v42
	v_cvt_pk_bf16_f32 v2, v2, v3
	ds_write_b16 v54, v2 offset:3328
	v_mul_f32_e32 v2, v34, v42
	v_cvt_pk_bf16_f32 v2, v2, v3
	v_ashrrev_i32_e32 v37, 31, v36
	ds_write_b16 v54, v2 offset:3392
	v_mul_f32_e32 v2, v19, v43
	v_lshl_add_u64 v[36:37], s[16:17], 0, v[36:37]
	v_cvt_pk_bf16_f32 v2, v2, v3
	v_lshlrev_b64 v[36:37], 10, v[36:37]
	ds_write_b16 v54, v2 offset:3456
	v_mul_f32_e32 v2, v35, v43
	v_cvt_pk_bf16_f32 v2, v2, v3
	ds_write_b16 v54, v2 offset:3520
	v_lshl_add_u64 v[4:5], s[12:13], 0, v[36:37]
	s_lshl_b32 s34, s51, 1
	v_lshrrev_b32_e32 v16, 3, v138
	v_add_u32_e32 v17, v44, v80
	v_lshl_add_u64 v[4:5], v[4:5], 0, s[34:35]
	s_waitcnt lgkmcnt(0)
	v_mov_b32_e32 v81, v3
	v_lshl_add_u32 v2, v16, 7, v17
	v_or_b32_e32 v18, 8, v16
	v_lshl_add_u64 v[12:13], v[4:5], 0, v[80:81]
	ds_read_b128 v[4:7], v2
	v_lshl_add_u32 v8, v18, 7, v17
	ds_read_b128 v[8:11], v8
	v_lshlrev_b32_e32 v2, 10, v16
	v_lshl_add_u64 v[14:15], v[12:13], 0, v[2:3]
	v_lshlrev_b32_e32 v2, 10, v18
	s_waitcnt lgkmcnt(1)
	global_store_dwordx4 v[14:15], v[4:7], off
	s_mov_b64 s[2:3], 0
	s_nop 0
	v_lshl_add_u64 v[4:5], v[12:13], 0, v[2:3]
	v_or_b32_e32 v2, 16, v16
	s_waitcnt lgkmcnt(0)
	global_store_dwordx4 v[4:5], v[8:11], off
	v_lshl_add_u32 v4, v2, 7, v17
	v_or_b32_e32 v16, 24, v16
	ds_read_b128 v[4:7], v4
	v_lshl_add_u32 v8, v16, 7, v17
	ds_read_b128 v[8:11], v8
	v_lshlrev_b32_e32 v2, 10, v2
	v_lshl_add_u64 v[14:15], v[12:13], 0, v[2:3]
	v_lshlrev_b32_e32 v2, 10, v16
	s_waitcnt lgkmcnt(1)
	global_store_dwordx4 v[14:15], v[4:7], off
	s_nop 1
	v_lshl_add_u64 v[4:5], v[12:13], 0, v[2:3]
	s_waitcnt lgkmcnt(0)
	global_store_dwordx4 v[4:5], v[8:11], off
	s_waitcnt lgkmcnt(0)
	s_barrier
